# v39 + P2 copy slots of the 10-unit groups spread evenly over the bf16 part (unit slots 0,0,1,1,2,2,3,3 instead of 0,0,1,1,2,3,3,4)
# speedup vs baseline: 1.0047x; 1.0011x over previous
.LBB0_196:
	s_ashr_i32 s5, s90, 4
	s_and_b32 s5, s5, -8
	s_and_b32 s6, s90, 7
	s_or_b32 s5, s5, s6
	s_mul_i32 s4, s4, s5
	s_ashr_i32 s5, s4, 31
	s_lshr_b32 s5, s5, 28
	s_add_i32 s4, s4, s5
	s_ashr_i32 s42, s4, 4
	s_and_b32 s6, s90, 7
	s_lshr_b32 s6, s6, 1
	s_cmp_lt_u32 s90, 0x80
	s_cselect_b32 s42, s6, s42
